# prep tile-to-block permutation: the 8 tiles of one XCD cover a contiguous 1KiB of each W row; rest as v40
# speedup vs baseline: 1.0075x; 1.0021x over previous
_Z11prep_kernelPKfS0_S0_S0_Pf:
	s_load_dwordx8 s[4:11], s[0:1], 0x0
	s_load_dwordx2 s[12:13], s[0:1], 0x20
	s_cmpk_eq_i32 s2, 0x100
	s_cbranch_scc1 .Lprep_exit
	s_and_b32 s14, s2, 7
	s_lshl_b32 s14, s14, 3
	s_bfe_u32 s16, s2, 0x30003
	s_or_b32 s14, s14, s16
	s_lshr_b32 s15, s2, 6
	v_and_b32_e32 v1, 7, v0
	v_and_b32_e32 v2, 0x3f8, v0
	v_lshlrev_b32_e32 v3, 10, v2
	v_lshl_or_b32 v3, v1, 4, v3
	s_lshl_b32 s16, s15, 21
	s_lshl_b32 s17, s14, 7
	s_add_i32 s16, s16, s17
	v_add_u32_e32 v3, s16, v3
	v_add_u32_e32 v4, 0x100000, v3
	v_lshrrev_b32_e32 v5, 1, v2
	s_lshl_b32 s18, s15, 10
	v_add_u32_e32 v5, s18, v5
	v_and_b32_e32 v19, 63, v0
	v_lshrrev_b32_e32 v20, 6, v0
	s_waitcnt lgkmcnt(0)
	global_load_dwordx4 v[8:11], v3, s[4:5] nt
	global_load_dwordx4 v[12:15], v4, s[4:5] nt
	global_load_dword v6, v5, s[6:7]
	global_load_dword v16, v5, s[6:7] offset:512
	s_cmp_lt_u32 s14, 32
	s_cbranch_scc0 .Lprep_ld_done
	v_cmp_gt_u32_e32 vcc, 0x200, v0
	s_and_saveexec_b64 s[20:21], vcc
	s_cbranch_execz .Lprep_hb_skip
	v_lshrrev_b32_e32 v17, 5, v0
	v_and_b32_e32 v18, 31, v0
	v_lshlrev_b32_e32 v17, 12, v17
	v_lshl_or_b32 v17, v18, 2, v17
	v_add_u32_e32 v17, s17, v17
	global_load_dword v36, v17, s[10:11]
